# hand-scheduled GQA inner loop (K reads up front, exps and LDS tile write under the PV MFMAs, tr reads early) on top of MLA loop rewrite
# speedup vs baseline: 1.0268x; 1.0154x over previous
; #define SBAR() __builtin_amdgcn_sched_barrier(0)
; template <bool FIXM> __device__ __forceinline__ void pv_psm(f32x16& o0, f32x16& o1, unsigned vb, bf16x8 pa0, bf16x8 pa1, bf16x8 pa2, bf16x8 pa3,
;                                        f32x16& p0, f32x16& p1, float& m_reg, f32x16& negm, float& alpha) {
;     { const s16x4 l0 = tr_read<v_rd_off(0, 0, 0)>(vb), h0 = tr_read<v_rd_off(0, 0, 1)>(vb), l1 = tr_read<v_rd_off(0, 1, 0)>(vb), h1 = tr_read<v_rd_off(0, 1, 1)>(vb);
;       const s16x4 l2 = tr_read<v_rd_off(0, 2, 0)>(vb), h2 = tr_read<v_rd_off(0, 2, 1)>(vb), l3 = tr_read<v_rd_off(0, 3, 0)>(vb), h3 = tr_read<v_rd_off(0, 3, 1)>(vb);
;       float pmax = 0.f; SBAR(); if (!FIXM) pmax = psm_max(p0, p1); else { _Pragma("unroll") for (int r = 0; r < 8; ++r) p0[r] = __builtin_amdgcn_exp2f(p0[r]); } SBAR();
;       asm volatile("s_waitcnt lgkmcnt(0)" ::: "memory"); SBAR();
;       o0 = __builtin_amdgcn_mfma_f32_32x32x16_bf16(ATT_PK(l0, h0), pa0, o0, 0, 0, 0);
;       o0 = __builtin_amdgcn_mfma_f32_32x32x16_bf16(ATT_PK(l1, h1), pa1, o0, 0, 0, 0);
;       o0 = __builtin_amdgcn_mfma_f32_32x32x16_bf16(ATT_PK(l2, h2), pa2, o0, 0, 0, 0);
;       o0 = __builtin_amdgcn_mfma_f32_32x32x16_bf16(ATT_PK(l3, h3), pa3, o0, 0, 0, 0);
;       SBAR();
;       const s16x4 m0 = tr_read<v_rd_off(1, 0, 0)>(vb), n0 = tr_read<v_rd_off(1, 0, 1)>(vb), m1 = tr_read<v_rd_off(1, 1, 0)>(vb), n1 = tr_read<v_rd_off(1, 1, 1)>(vb);
;       const s16x4 m2 = tr_read<v_rd_off(1, 2, 0)>(vb), n2 = tr_read<v_rd_off(1, 2, 1)>(vb), m3 = tr_read<v_rd_off(1, 3, 0)>(vb), n3 = tr_read<v_rd_off(1, 3, 1)>(vb);
;       SBAR(); if (!FIXM) psm_apply<false>(p0, p1, pmax, m_reg, negm, alpha); else { alpha = 1.f; _Pragma("unroll") for (int r = 8; r < 16; ++r) p0[r] = __builtin_amdgcn_exp2f(p0[r]); } SBAR();
;       asm volatile("s_waitcnt lgkmcnt(0)" ::: "memory"); SBAR();
;       o1 = __builtin_amdgcn_mfma_f32_32x32x16_bf16(ATT_PK(m0, n0), pa0, o1, 0, 0, 0);
; template <int DQK, bool FIXM> ...
;     ...
;         SBAR(); qkt<DQK>(pB0, pB1, lds + bK, qr, r32, hi, negm);
;         finishSM(pA0, pA1, alA, l_reg, pa0, pa1, pa2, pa3); SBAR();
;         SLOAD(1, j + 2); SBAR();
;         if constexpr (FIXM) pv_psm<true>(o0, o1, vb0 + bV, pa0, pa1, pa2, pa3, pB0, pB1, m_reg, negm, alB); else { PVO(bV); partialSM<false>(pB0, pB1, m_reg, negm, alB); }
;         SWAIT(); SWRITEO(bW, 0);
;         if (!FIXM) RESC(alB); ROT();
.LBB0_497:
	s_mov_b32 s1, s11
	s_mov_b32 s11, s35
	s_waitcnt lgkmcnt(0)
	s_barrier
	v_add_u32_e32 v252, s1, v208
	v_add_u32_e32 v228, v252, v209
	ds_read_b128 v[224:227], v228
	ds_read_b128 v[228:231], v228 offset:4096
	v_add_u32_e32 v236, v252, v210
	ds_read_b128 v[232:235], v236
	ds_read_b128 v[236:239], v236 offset:4096
	v_add_u32_e32 v244, v252, v211
	ds_read_b128 v[240:243], v244
	ds_read_b128 v[244:247], v244 offset:4096
	v_add_u32_e32 v253, v252, v212
	ds_read_b128 v[248:251], v253
	v_exp_f32_e32 v66, v66
	v_exp_f32_e32 v67, v67
	v_exp_f32_e32 v68, v68
	v_exp_f32_e32 v69, v69
	v_exp_f32_e32 v70, v70
	v_exp_f32_e32 v71, v71
	v_exp_f32_e32 v72, v72
	v_exp_f32_e32 v73, v73
	s_waitcnt lgkmcnt(6)
	v_mfma_f32_32x32x16_bf16 v[98:113], v[224:227], v[114:117], v[18:33]
	ds_read_b128 v[224:227], v253 offset:4096
	v_exp_f32_e32 v74, v74
	v_exp_f32_e32 v75, v75
	v_exp_f32_e32 v76, v76
	v_cvt_pk_bf16_f32 v156, v143, v145
	v_cvt_pk_bf16_f32 v157, v141, v144
	v_add_f32_e32 v164, 0, v143
	v_add_f32_e32 v164, v145, v164
	v_add_f32_e32 v164, v141, v164
	s_waitcnt lgkmcnt(6)
	v_mfma_f32_32x32x16_bf16 v[82:97], v[228:231], v[114:117], v[18:33]
	v_exp_f32_e32 v77, v77
	v_exp_f32_e32 v78, v78
	v_exp_f32_e32 v79, v79
	v_cvt_pk_bf16_f32 v158, v139, v142
	v_cvt_pk_bf16_f32 v159, v138, v140
	v_add_f32_e32 v164, v144, v164
	v_add_f32_e32 v164, v139, v164
	v_add_f32_e32 v164, v142, v164
	s_waitcnt lgkmcnt(5)
	v_mfma_f32_32x32x16_bf16 v[98:113], v[232:235], v[12:15], v[98:113]
	v_exp_f32_e32 v80, v80
	v_exp_f32_e32 v81, v81
	v_cvt_pk_bf16_f32 v160, v151, v153
	v_cvt_pk_bf16_f32 v161, v149, v152
	v_cvt_pk_bf16_f32 v162, v147, v150
	v_cvt_pk_bf16_f32 v163, v146, v148
	v_add_f32_e32 v164, v138, v164
	v_add_f32_e32 v164, v140, v164
	v_add_f32_e32 v164, v151, v164
	s_waitcnt lgkmcnt(4)
	v_mfma_f32_32x32x16_bf16 v[82:97], v[236:239], v[12:15], v[82:97]
	v_add_f32_e32 v164, v153, v164
	v_add_f32_e32 v164, v149, v164
	v_add_f32_e32 v164, v152, v164
	v_add_f32_e32 v164, v147, v164
	v_add_f32_e32 v164, v150, v164
	v_add_f32_e32 v164, v146, v164
	v_add_f32_e32 v164, v148, v164
	s_waitcnt lgkmcnt(3)
	v_mfma_f32_32x32x16_bf16 v[98:113], v[240:243], v[8:11], v[98:113]
	v_add_u32_e32 v2, s11, v213
	ds_read_b64_tr_b16 v[138:139], v2 offset:0
	ds_read_b64_tr_b16 v[140:141], v2 offset:1024
	ds_read_b64_tr_b16 v[142:143], v2 offset:2048
	ds_read_b64_tr_b16 v[144:145], v2 offset:3072
	v_add_f32_e32 v164, v66, v164
	v_add_f32_e32 v164, v67, v164
	v_add_f32_e32 v164, v68, v164
	v_add_f32_e32 v164, v69, v164
	s_waitcnt lgkmcnt(6)
	v_mfma_f32_32x32x16_bf16 v[82:97], v[244:247], v[8:11], v[82:97]
	ds_read_b64_tr_b16 v[146:147], v2 offset:4096
	ds_read_b64_tr_b16 v[148:149], v2 offset:5120
	ds_read_b64_tr_b16 v[150:151], v2 offset:6144
	ds_read_b64_tr_b16 v[152:153], v2 offset:7168
	v_add_f32_e32 v164, v70, v164
	v_add_f32_e32 v164, v71, v164
	v_add_f32_e32 v164, v72, v164
	v_add_f32_e32 v164, v73, v164
	s_waitcnt lgkmcnt(9)
	v_mfma_f32_32x32x16_bf16 v[98:113], v[248:251], v[4:7], v[98:113]
	v_add_f32_e32 v164, v74, v164
	v_add_f32_e32 v164, v75, v164
	v_add_f32_e32 v164, v76, v164
	v_add_f32_e32 v164, v77, v164
	s_add_i32 s8, s13, -1
	s_cmp_lt_u32 s8, s31
	s_cselect_b32 s9, 0, s31
	s_cselect_b32 s35, s12, s29
	s_lshl_b32 s9, s9, 6
	s_sub_i32 s9, s35, s9
	s_waitcnt lgkmcnt(8)
	v_mfma_f32_32x32x16_bf16 v[82:97], v[224:227], v[4:7], v[82:97]
	v_add_u32_e32 v252, s9, v137
	v_subrev_u32_e32 v126, 64, v252
	v_ashrrev_i32_e32 v127, 31, v126
	v_lshlrev_b64 v[126:127], 8, v[126:127]
	v_lshl_add_u64 v[128:129], v[16:17], 0, v[126:127]
	v_lshl_add_u64 v[126:127], v[134:135], 0, v[126:127]
	global_load_dwordx4 v[130:133], v[128:129], off
	s_nop 0
	global_load_dwordx4 v[126:129], v[126:127], off
	ds_read_b64_tr_b16 v[224:225], v2 offset:512
	ds_read_b64_tr_b16 v[226:227], v2 offset:1536
	ds_read_b64_tr_b16 v[228:229], v2 offset:2560
	ds_read_b64_tr_b16 v[230:231], v2 offset:3584
	ds_read_b64_tr_b16 v[232:233], v2 offset:4608
	ds_read_b64_tr_b16 v[234:235], v2 offset:5632
	ds_read_b64_tr_b16 v[236:237], v2 offset:6656
	ds_read_b64_tr_b16 v[238:239], v2 offset:7680
	s_waitcnt lgkmcnt(8)
	v_mfma_f32_32x32x16_bf16 v[50:65], v[138:141], v[156:159], v[50:65]
	v_add_f32_e32 v164, v78, v164
	v_add_f32_e32 v164, v79, v164
	v_add_f32_e32 v164, v80, v164
	v_add_f32_e32 v154, v81, v164
	v_mov_b32_e32 v155, v154
	v_mfma_f32_32x32x16_bf16 v[50:65], v[142:145], v[160:163], v[50:65]
	v_cvt_pk_bf16_f32 v66, v66, v67
	v_cvt_pk_bf16_f32 v67, v68, v69
	v_cvt_pk_bf16_f32 v68, v70, v71
	v_cvt_pk_bf16_f32 v69, v72, v73
	v_cvt_pk_bf16_f32 v70, v74, v75
	v_cvt_pk_bf16_f32 v71, v76, v77
	v_cvt_pk_bf16_f32 v72, v78, v79
	v_cvt_pk_bf16_f32 v73, v80, v81
	v_permlane32_swap_b32_e32 v154, v155
	v_mfma_f32_32x32x16_bf16 v[50:65], v[146:149], v[66:69], v[50:65]
	v_mfma_f32_32x32x16_bf16 v[50:65], v[150:153], v[70:73], v[50:65]
	s_waitcnt lgkmcnt(0)
	v_mfma_f32_32x32x16_bf16 v[34:49], v[224:227], v[156:159], v[34:49]
	s_waitcnt vmcnt(2)
	v_add_u32_e32 v165, s10, v187
	ds_write_b128 v165, v[118:121]
	v_add_u32_e32 v165, s10, v214
	ds_write_b128 v165, v[122:125] offset:12288
	v_exp_f32_e32 v168, v98
	v_exp_f32_e32 v169, v99
	v_mfma_f32_32x32x16_bf16 v[34:49], v[228:231], v[160:163], v[34:49]
	v_exp_f32_e32 v170, v100
	v_exp_f32_e32 v171, v101
	v_exp_f32_e32 v172, v102
	v_exp_f32_e32 v173, v103
	v_mfma_f32_32x32x16_bf16 v[34:49], v[232:235], v[66:69], v[34:49]
	v_exp_f32_e32 v174, v104
	v_exp_f32_e32 v175, v105
	v_exp_f32_e32 v176, v106
	v_exp_f32_e32 v177, v107
	v_exp_f32_e32 v178, v108
	v_mfma_f32_32x32x16_bf16 v[34:49], v[236:239], v[70:73], v[34:49]
	v_exp_f32_e32 v179, v109
	v_exp_f32_e32 v180, v110
	v_exp_f32_e32 v181, v111
	v_exp_f32_e32 v182, v112
	v_exp_f32_e32 v183, v113
	s_waitcnt lgkmcnt(0)
	s_barrier
; #define SBAR() __builtin_amdgcn_sched_barrier(0)
; template <bool FIXM> __device__ __forceinline__ void pv_psm(f32x16& o0, f32x16& o1, unsigned vb, bf16x8 pa0, bf16x8 pa1, bf16x8 pa2, bf16x8 pa3,
;                                        f32x16& p0, f32x16& p1, float& m_reg, f32x16& negm, float& alpha) {
;     { const s16x4 l0 = tr_read<v_rd_off(0, 0, 0)>(vb), h0 = tr_read<v_rd_off(0, 0, 1)>(vb), l1 = tr_read<v_rd_off(0, 1, 0)>(vb), h1 = tr_read<v_rd_off(0, 1, 1)>(vb);
;       const s16x4 l2 = tr_read<v_rd_off(0, 2, 0)>(vb), h2 = tr_read<v_rd_off(0, 2, 1)>(vb), l3 = tr_read<v_rd_off(0, 3, 0)>(vb), h3 = tr_read<v_rd_off(0, 3, 1)>(vb);
;       float pmax = 0.f; SBAR(); if (!FIXM) pmax = psm_max(p0, p1); else { _Pragma("unroll") for (int r = 0; r < 8; ++r) p0[r] = __builtin_amdgcn_exp2f(p0[r]); } SBAR();
;       asm volatile("s_waitcnt lgkmcnt(0)" ::: "memory"); SBAR();
;       o0 = __builtin_amdgcn_mfma_f32_32x32x16_bf16(ATT_PK(l0, h0), pa0, o0, 0, 0, 0);
;       o0 = __builtin_amdgcn_mfma_f32_32x32x16_bf16(ATT_PK(l1, h1), pa1, o0, 0, 0, 0);
;       o0 = __builtin_amdgcn_mfma_f32_32x32x16_bf16(ATT_PK(l2, h2), pa2, o0, 0, 0, 0);
;       o0 = __builtin_amdgcn_mfma_f32_32x32x16_bf16(ATT_PK(l3, h3), pa3, o0, 0, 0, 0);
;       SBAR();
;       const s16x4 m0 = tr_read<v_rd_off(1, 0, 0)>(vb), n0 = tr_read<v_rd_off(1, 0, 1)>(vb), m1 = tr_read<v_rd_off(1, 1, 0)>(vb), n1 = tr_read<v_rd_off(1, 1, 1)>(vb);
;       const s16x4 m2 = tr_read<v_rd_off(1, 2, 0)>(vb), n2 = tr_read<v_rd_off(1, 2, 1)>(vb), m3 = tr_read<v_rd_off(1, 3, 0)>(vb), n3 = tr_read<v_rd_off(1, 3, 1)>(vb);
;       SBAR(); if (!FIXM) psm_apply<false>(p0, p1, pmax, m_reg, negm, alpha); else { alpha = 1.f; _Pragma("unroll") for (int r = 8; r < 16; ++r) p0[r] = __builtin_amdgcn_exp2f(p0[r]); } SBAR();
;       asm volatile("s_waitcnt lgkmcnt(0)" ::: "memory"); SBAR();
; template <int DQK, bool FIXM> ...
;     ...
;         if (!NOBAR_PROBE) __syncthreads();
;         SBAR(); qkt<DQK>(pA0, pA1, lds + bK, qr, r32, hi, negm);
;         finishSM(pB0, pB1, alB, l_reg, pa0, pa1, pa2, pa3); SBAR();
;         if (j + 3 < NT) SLOAD(0, j + 3); SBAR();
;         if constexpr (FIXM) pv_psm<true>(o0, o1, vb0 + bV, pa0, pa1, pa2, pa3, pA0, pA1, m_reg, negm, alA); else { PVO(bV); partialSM<false>(pA0, pA1, m_reg, negm, alA); }
;         SWAIT(); SWRITEO(bW, 1);
;         if (!FIXM) RESC(alA); ROT();
	v_add_u32_e32 v252, s10, v201
	v_add_u32_e32 v228, v252, v209
	ds_read_b128 v[224:227], v228
	ds_read_b128 v[228:231], v228 offset:4096
	v_add_u32_e32 v236, v252, v210
	ds_read_b128 v[232:235], v236
	ds_read_b128 v[236:239], v236 offset:4096
	v_add_u32_e32 v244, v252, v211
	ds_read_b128 v[240:243], v244
	ds_read_b128 v[244:247], v244 offset:4096
	v_add_u32_e32 v253, v252, v212
	ds_read_b128 v[248:251], v253
	v_exp_f32_e32 v82, v82
	v_exp_f32_e32 v83, v83
	v_exp_f32_e32 v84, v84
	v_exp_f32_e32 v85, v85
	v_exp_f32_e32 v86, v86
	v_exp_f32_e32 v87, v87
	v_exp_f32_e32 v88, v88
	v_exp_f32_e32 v89, v89
	s_waitcnt lgkmcnt(6)
	v_mfma_f32_32x32x16_bf16 v[98:113], v[224:227], v[114:117], v[18:33]
	ds_read_b128 v[224:227], v253 offset:4096
	v_exp_f32_e32 v90, v90
	v_exp_f32_e32 v91, v91
	v_exp_f32_e32 v92, v92
	v_cvt_pk_bf16_f32 v156, v168, v169
	v_cvt_pk_bf16_f32 v157, v170, v171
	v_add_f32_e32 v164, 0, v168
	v_add_f32_e32 v164, v169, v164
	v_add_f32_e32 v164, v170, v164
	s_waitcnt lgkmcnt(6)
	v_mfma_f32_32x32x16_bf16 v[66:81], v[228:231], v[114:117], v[18:33]
	v_exp_f32_e32 v93, v93
	v_exp_f32_e32 v94, v94
	v_exp_f32_e32 v95, v95
	v_cvt_pk_bf16_f32 v158, v172, v173
	v_cvt_pk_bf16_f32 v159, v174, v175
	v_add_f32_e32 v164, v171, v164
	v_add_f32_e32 v164, v172, v164
	v_add_f32_e32 v164, v173, v164
	s_waitcnt lgkmcnt(5)
	v_mfma_f32_32x32x16_bf16 v[98:113], v[232:235], v[12:15], v[98:113]
	v_exp_f32_e32 v96, v96
	v_exp_f32_e32 v97, v97
	v_cvt_pk_bf16_f32 v160, v176, v177
	v_cvt_pk_bf16_f32 v161, v178, v179
	v_cvt_pk_bf16_f32 v162, v180, v181
	v_cvt_pk_bf16_f32 v163, v182, v183
	v_add_f32_e32 v164, v174, v164
	v_add_f32_e32 v164, v175, v164
	v_add_f32_e32 v164, v176, v164
	s_waitcnt lgkmcnt(4)
	v_mfma_f32_32x32x16_bf16 v[66:81], v[236:239], v[12:15], v[66:81]
	v_add_f32_e32 v164, v177, v164
	v_add_f32_e32 v164, v178, v164
	v_add_f32_e32 v164, v179, v164
	v_add_f32_e32 v164, v180, v164
	v_add_f32_e32 v164, v181, v164
	v_add_f32_e32 v164, v182, v164
	v_add_f32_e32 v164, v183, v164
	s_waitcnt lgkmcnt(3)
	v_mfma_f32_32x32x16_bf16 v[98:113], v[240:243], v[8:11], v[98:113]
	v_add_u32_e32 v253, s1, v213
	ds_read_b64_tr_b16 v[168:169], v253 offset:0
	ds_read_b64_tr_b16 v[170:171], v253 offset:1024
	ds_read_b64_tr_b16 v[172:173], v253 offset:2048
	ds_read_b64_tr_b16 v[174:175], v253 offset:3072
	v_add_f32_e32 v164, v82, v164
	v_add_f32_e32 v164, v83, v164
	v_add_f32_e32 v164, v84, v164
	v_add_f32_e32 v164, v85, v164
	s_waitcnt lgkmcnt(6)
	v_mfma_f32_32x32x16_bf16 v[66:81], v[244:247], v[8:11], v[66:81]
	ds_read_b64_tr_b16 v[176:177], v253 offset:4096
	ds_read_b64_tr_b16 v[178:179], v253 offset:5120
	ds_read_b64_tr_b16 v[180:181], v253 offset:6144
	ds_read_b64_tr_b16 v[182:183], v253 offset:7168
	v_add_f32_e32 v164, v86, v164
	v_add_f32_e32 v164, v87, v164
	v_add_f32_e32 v164, v88, v164
	v_add_f32_e32 v164, v89, v164
	s_waitcnt lgkmcnt(9)
	v_mfma_f32_32x32x16_bf16 v[98:113], v[248:251], v[4:7], v[98:113]
	v_add_f32_e32 v164, v90, v164
	v_add_f32_e32 v164, v91, v164
	v_add_f32_e32 v164, v92, v164
	v_add_f32_e32 v164, v93, v164
	s_waitcnt lgkmcnt(8)
	v_mfma_f32_32x32x16_bf16 v[66:81], v[224:227], v[4:7], v[66:81]
	s_cmp_ge_u32 s13, s30
	s_cbranch_scc1 .Lgqa_b_noload
	s_cmp_lt_u32 s13, s31
	s_cselect_b32 s9, 0, s31
	s_cselect_b32 s35, s12, s29
	s_lshl_b32 s9, s9, 6
	s_sub_i32 s9, s35, s9
	v_add_u32_e32 v118, s9, v137
	v_ashrrev_i32_e32 v119, 31, v118
	v_lshlrev_b64 v[118:119], 8, v[118:119]
	v_lshl_add_u64 v[120:121], v[16:17], 0, v[118:119]
	v_lshl_add_u64 v[122:123], v[134:135], 0, v[118:119]
	global_load_dwordx4 v[118:121], v[120:121], off
	s_nop 0
	global_load_dwordx4 v[122:125], v[122:123], off
.Lgqa_b_ld_done:
	ds_read_b64_tr_b16 v[224:225], v253 offset:512
	ds_read_b64_tr_b16 v[226:227], v253 offset:1536
	ds_read_b64_tr_b16 v[228:229], v253 offset:2560
	ds_read_b64_tr_b16 v[230:231], v253 offset:3584
	ds_read_b64_tr_b16 v[232:233], v253 offset:4608
	ds_read_b64_tr_b16 v[234:235], v253 offset:5632
	ds_read_b64_tr_b16 v[236:237], v253 offset:6656
	ds_read_b64_tr_b16 v[238:239], v253 offset:7680
	s_waitcnt lgkmcnt(8)
	v_mfma_f32_32x32x16_bf16 v[50:65], v[168:171], v[156:159], v[50:65]
	v_add_f32_e32 v164, v94, v164
	v_add_f32_e32 v164, v95, v164
	v_add_f32_e32 v164, v96, v164
	v_add_f32_e32 v164, v97, v164
	v_mov_b32_e32 v165, v164
	v_mfma_f32_32x32x16_bf16 v[50:65], v[172:175], v[160:163], v[50:65]
	v_cvt_pk_bf16_f32 v82, v82, v83
	v_cvt_pk_bf16_f32 v83, v84, v85
	v_cvt_pk_bf16_f32 v84, v86, v87
	v_cvt_pk_bf16_f32 v85, v88, v89
	v_cvt_pk_bf16_f32 v86, v90, v91
	v_cvt_pk_bf16_f32 v87, v92, v93
	v_cvt_pk_bf16_f32 v88, v94, v95
	v_cvt_pk_bf16_f32 v89, v96, v97
	v_permlane32_swap_b32_e32 v164, v165
	v_mfma_f32_32x32x16_bf16 v[50:65], v[176:179], v[82:85], v[50:65]
	v_mfma_f32_32x32x16_bf16 v[50:65], v[180:183], v[86:89], v[50:65]
	s_waitcnt lgkmcnt(0)
	v_mfma_f32_32x32x16_bf16 v[34:49], v[224:227], v[156:159], v[34:49]
	s_waitcnt vmcnt(2)
	v_add_u32_e32 v252, s11, v187
	ds_write_b128 v252, v[130:133]
	v_add_u32_e32 v252, s11, v214
	ds_write_b128 v252, v[126:129] offset:12288
	v_exp_f32_e32 v143, v98
	v_exp_f32_e32 v145, v99
	v_mfma_f32_32x32x16_bf16 v[34:49], v[228:231], v[160:163], v[34:49]
	v_exp_f32_e32 v141, v100
	v_exp_f32_e32 v144, v101
	v_exp_f32_e32 v139, v102
	v_exp_f32_e32 v142, v103
	v_mfma_f32_32x32x16_bf16 v[34:49], v[232:235], v[82:85], v[34:49]
	v_exp_f32_e32 v138, v104
	v_exp_f32_e32 v140, v105
	v_exp_f32_e32 v151, v106
	v_exp_f32_e32 v153, v107
	v_exp_f32_e32 v149, v108
	v_mfma_f32_32x32x16_bf16 v[34:49], v[236:239], v[86:89], v[34:49]
	v_exp_f32_e32 v152, v109
	v_exp_f32_e32 v147, v110
	v_exp_f32_e32 v150, v111
	v_exp_f32_e32 v146, v112
	v_exp_f32_e32 v148, v113
	v_add_f32_e32 v252, v154, v155
	v_add_f32_e32 v136, v136, v252
	v_add_f32_e32 v252, v164, v165
	v_add_f32_e32 v136, v136, v252
	s_mov_b32 s9, s11
	s_add_i32 s13, s13, 2
	v_add_u32_e32 v137, 0x80, v137
	s_cmp_lt_u32 s8, s0
	s_cbranch_scc0 .Lgqa_exit
	s_mov_b32 s35, s10
	s_mov_b32 s10, s1
	s_branch .LBB0_497

; #define SBAR() __builtin_amdgcn_sched_barrier(0)
; #define PVO(boff) do { pv_one<0>(o0, vb0 + (boff), pa0, pa1, pa2, pa3); pv_one<1>(o1, vb0 + (boff), pa0, pa1, pa2, pa3); } while (0)
; #define RESC(a) do { if (__any((a) < 1.f)) { _Pragma("unroll") for (int r = 0; r < 16; ++r) { o0[r] *= (a); o1[r] *= (a); } } } while (0)
; template <int DQK, bool FIXM> ...
;     ...
;     __syncthreads();
;     SBAR(); qkt<DQK>(pB0, pB1, lds + bK, qr, r32, hi, negm);
;     finishSM(pA0, pA1, alA, l_reg, pa0, pa1, pa2, pa3); SBAR();
;     if constexpr (FIXM) pv_psm<true>(o0, o1, vb0 + bV, pa0, pa1, pa2, pa3, pB0, pB1, m_reg, negm, alB); else { PVO(bV); partialSM<false>(pB0, pB1, m_reg, negm, alB); }
;     if (!FIXM) RESC(alB);
;     finishSM(pB0, pB1, alB, l_reg, pa0, pa1, pa2, pa3); SBAR();
;     PVO(bK);
.Lgqa_exit:
	v_add_u32_e32 v2, s11, v213
	s_branch .LBB0_501

; __device__ __forceinline__ int v_st(int k, int c) { const int kk = k;     return ((kk >> 3) * 2 + (c >> 5)) * 512 + ((kk & 7) * 32 + (c & 31)) * 2; }
; __device__ __forceinline__ int v_rd_base(int lane) { return ((lane & 3) << 3) | (((lane >> 2) & 3) << 6) | (((lane >> 4) & 1) << 5) | (((lane >> 5) & 1) << 8); }
; #define SLOAD(i, j) do { const int _row = KROW(j); skn[i] = *(const bf16x8*)(Knp + (size_t)(_row + sr) * ldk + c8 * 8); sv[i] = *(const bf16x8*)(Vp + (size_t)(_row + sr) * ldv + c8 * 8); \
;         if (krw) skr[i] = *(const bf16x8*)(Krp + (size_t)(_row + sr2) * 32 + c4 * 8); } while (0)
; #define SWRITE(b, i) do { *(LAS bf16x8*)(lds + (b) * BUF + kn_st) = skn[i]; *(LAS bf16x8*)(lds + (b) * BUF + v_stw) = sv[i]; if (krw) *(LAS bf16x8*)(lds + (b) * BUF + kr_st) = skr[i]; } while (0)
; #define SWRITEO(boff, i) do { *(LAS bf16x8*)(lds + (boff) + kn_st) = skn[i]; *(LAS bf16x8*)(lds + (boff) + v_stw) = sv[i]; if (krw) *(LAS bf16x8*)(lds + (boff) + kr_st) = skr[i]; } while (0)
; #define SWAIT() asm volatile("s_waitcnt vmcnt(2)" ::: "memory")
; template <int DQK, bool FIXM> ...
;     ...
;     const int sr = tid >> 3, c8 = tid & 7, sr2 = (tid >> 2) & 63, c4 = tid & 3;
;     const bool krw = (DQK == 96) && (tid < 256);
;     const int kn_st = B_KN + swz64(sr, c8), v_stw = B_V + v_st(sr, c8 * 8), kr_st = B_KR + swz32(sr2, c4);
;     const unsigned vb0 = (unsigned)(uintptr_t)lds + B_V + v_rd_base(lane);
;     bf16x8 skn[2], sv[2], skr[2];
;     ...
;     __syncthreads();
;     SLOAD(0, 0); asm volatile("s_waitcnt vmcnt(0)" ::: "memory"); SWRITE(0, 0);
;     SLOAD(1, 1); if (2 < NT) SLOAD(0, 2);
;     __syncthreads();
;     qkt<DQK>(pA0, pA1, lds, qr, r32, hi, negm);
;     if (FIXM) { alA = 1.f; _Pragma("unroll") for (int r = 0; r < 16; ++r) pA0[r] = __builtin_amdgcn_exp2f(pA0[r]); } else partialSM<true>(pA0, pA1, m_reg, negm, alA);
;     SWAIT(); SWRITEO(BUF, 1);
.LBB0_520:
	s_or_b64 exec, exec, s[0:1]
	v_add_u32_e32 v15, v208, v209
	s_waitcnt lgkmcnt(0)
	s_barrier
	ds_read_b128 v[34:37], v15
	ds_read_b128 v[38:41], v15 offset:4096
	s_waitcnt lgkmcnt(1)
	v_mfma_f32_32x32x16_bf16 v[50:65], v[34:37], v[166:169], 0
	v_add_u32_e32 v15, v208, v210
	ds_read_b128 v[66:69], v15
	ds_read_b128 v[70:73], v15 offset:4096
	v_add_u32_e32 v15, v208, v211
	s_waitcnt lgkmcnt(2)
	v_mfma_f32_32x32x16_bf16 v[34:49], v[38:41], v[166:169], 0
	s_waitcnt lgkmcnt(1)
	v_mfma_f32_32x32x16_bf16 v[50:65], v[66:69], v[162:165], v[50:65]
	s_waitcnt lgkmcnt(0)
	v_mfma_f32_32x32x16_bf16 v[34:49], v[70:73], v[162:165], v[34:49]
	ds_read_b128 v[66:69], v15
	ds_read_b128 v[70:73], v15 offset:4096
	v_add_u32_e32 v15, v208, v212
	s_waitcnt lgkmcnt(1)
	v_mfma_f32_32x32x16_bf16 v[50:65], v[66:69], v[158:161], v[50:65]
	s_waitcnt lgkmcnt(0)
	v_mfma_f32_32x32x16_bf16 v[34:49], v[70:73], v[158:161], v[34:49]
	ds_read_b128 v[66:69], v15
	ds_read_b128 v[70:73], v15 offset:4096
	v_add_u32_e32 v15, v218, v219
	s_waitcnt lgkmcnt(1)
	v_mfma_f32_32x32x16_bf16 v[50:65], v[66:69], v[154:157], v[50:65]
	s_waitcnt lgkmcnt(0)
	v_mfma_f32_32x32x16_bf16 v[34:49], v[70:73], v[154:157], v[34:49]
	ds_read_b128 v[66:69], v15 offset:8192
	ds_read_b128 v[70:73], v15 offset:10240
	v_add_u32_e32 v15, v218, v220
	s_waitcnt lgkmcnt(1)
	v_mfma_f32_32x32x16_bf16 v[50:65], v[66:69], v[150:153], v[50:65]
	ds_read_b128 v[66:69], v15 offset:8192
	ds_read_b128 v[74:77], v15 offset:10240
	s_waitcnt vmcnt(2)
	s_waitcnt vmcnt(3)
	ds_write_b128 v13, v[4:7] offset:20480
	s_waitcnt vmcnt(2)
	ds_write_b128 v14, v[8:11] offset:32768
	s_waitcnt lgkmcnt(3)
	v_mfma_f32_32x32x16_bf16 v[50:65], v[66:69], v[146:149], v[50:65]
	v_mfma_f32_32x32x16_bf16 v[34:49], v[70:73], v[150:153], v[34:49]
	s_nop 10
	v_max_f32_e32 v15, v51, v51
	v_max_f32_e32 v16, v50, v50
	v_max_f32_e32 v15, v16, v15
	v_max3_f32 v15, v15, v52, v53
	v_max3_f32 v15, v15, v54, v55
	v_max3_f32 v15, v15, v56, v57
	v_max3_f32 v15, v15, v58, v59
	s_waitcnt lgkmcnt(2)
	v_mfma_f32_32x32x16_bf16 v[34:49], v[74:77], v[146:149], v[34:49]
	v_max3_f32 v15, v15, v60, v61
	v_max3_f32 v15, v15, v62, v63
	v_max3_f32 v15, v15, v64, v65
	s_nop 8
	v_max3_f32 v15, v15, v34, v35
	v_max3_f32 v15, v15, v36, v37
	v_max3_f32 v15, v15, v38, v39
	v_max3_f32 v15, v15, v40, v41
	v_max3_f32 v15, v15, v42, v43
	v_max3_f32 v15, v15, v44, v45
	v_max3_f32 v15, v15, v46, v47
	v_max3_f32 v15, v15, v48, v49
	v_mov_b32_e32 v16, v15
	s_nop 1
	v_permlane32_swap_b32_e32 v15, v16
	s_and_saveexec_b64 s[0:1], s[2:3]
	ds_write_b128 v12, v[174:177] offset:28672
	s_or_b64 exec, exec, s[0:1]
	v_max_f32_e32 v4, v16, v16
	v_max_f32_e32 v5, v15, v15
	v_max_f32_e32 v4, v5, v4
	v_sub_f32_e32 v5, v50, v4
	v_sub_f32_e32 v6, v51, v4
	v_sub_f32_e32 v7, v52, v4
	v_sub_f32_e32 v8, v53, v4
	v_sub_f32_e32 v9, v54, v4
	v_sub_f32_e32 v10, v55, v4
	v_sub_f32_e32 v11, v56, v4
	v_sub_f32_e32 v12, v57, v4
	v_sub_f32_e32 v13, v58, v4
	v_sub_f32_e32 v14, v59, v4
	v_sub_f32_e32 v15, v60, v4
	v_sub_f32_e32 v16, v61, v4
	v_sub_f32_e32 v17, v62, v4
	v_sub_f32_e32 v50, v63, v4
	v_sub_f32_e32 v51, v64, v4
	v_sub_f32_e32 v52, v65, v4
	v_exp_f32_e32 v243, v5
	v_exp_f32_e32 v245, v6
	v_exp_f32_e32 v241, v7
	v_exp_f32_e32 v244, v8
	v_exp_f32_e32 v239, v9
	v_exp_f32_e32 v242, v10
	v_exp_f32_e32 v238, v11
	v_exp_f32_e32 v240, v12
	v_exp_f32_e32 v236, v13
	v_exp_f32_e32 v237, v14
	v_exp_f32_e32 v233, v15
	v_exp_f32_e32 v235, v16
	v_exp_f32_e32 v231, v17
	v_exp_f32_e32 v234, v50
	v_exp_f32_e32 v230, v51
	v_exp_f32_e32 v232, v52
	v_add_f32_e32 v224, 0, v4
	v_mov_b32_e32 v16, v3
	v_mov_b32_e32 v17, v3
	v_xor_b32_e32 v82, 0x80000000, v224
	v_sub_f32_e32 v113, v49, v4
	v_sub_f32_e32 v112, v48, v4
	v_sub_f32_e32 v111, v47, v4
	v_sub_f32_e32 v110, v46, v4
	v_sub_f32_e32 v109, v45, v4
	v_sub_f32_e32 v108, v44, v4
	v_sub_f32_e32 v107, v43, v4
	v_sub_f32_e32 v106, v42, v4
	v_sub_f32_e32 v105, v41, v4
	v_sub_f32_e32 v104, v40, v4
	v_sub_f32_e32 v103, v39, v4
	v_sub_f32_e32 v102, v38, v4
	v_sub_f32_e32 v101, v37, v4
	v_sub_f32_e32 v100, v36, v4
	v_sub_f32_e32 v99, v35, v4
	v_sub_f32_e32 v98, v34, v4
	v_lshl_add_u64 v[206:207], s[10:11], 0, v[2:3]
	s_mov_b64 s[42:43], s[10:11]
	v_mov_b32_e32 v2, v3
	v_mov_b32_e32 v4, v3
	v_mov_b32_e32 v5, v3
	v_mov_b32_e32 v6, v3
	v_mov_b32_e32 v7, v3
	v_mov_b32_e32 v8, v3
	v_mov_b32_e32 v9, v3
	v_mov_b32_e32 v10, v3
	v_mov_b32_e32 v11, v3
	v_mov_b32_e32 v12, v3
	v_mov_b32_e32 v13, v3
	v_mov_b32_e32 v14, v3
	v_mov_b32_e32 v15, v3
	v_mov_b64_e32 v[48:49], v[16:17]
	v_mov_b64_e32 v[64:65], v[16:17]
	s_ashr_i32 s9, s8, 31
	s_add_i32 s12, s31, -1
	s_mov_b32 s11, 0
	v_mov_b32_e32 v223, 0
	v_mov_b32_e32 v227, 1.0
	s_movk_i32 s13, 0x5000
	s_mov_b32 s0, 0xa000
	s_mov_b32 s35, 4
	v_readlane_b32 s44, v254, 8
	v_readlane_b32 s45, v254, 9
	s_nop 3
	s_add_u32 s44, s44, 0x1ea00000
	s_addc_u32 s45, s45, 0
	v_subrev_u32_e32 v225, s42, v206
	v_lshlrev_b32_e32 v226, 11, v221
	v_add_u32_e32 v225, v225, v226
	v_add_u32_e32 v225, 0xfff80000, v225
	v_subrev_u32_e32 v226, s44, v204
	v_lshl_add_u32 v226, v215, 6, v226
	v_mov_b64_e32 v[46:47], v[14:15]
	v_mov_b64_e32 v[44:45], v[12:13]
	v_mov_b64_e32 v[42:43], v[10:11]
	v_mov_b64_e32 v[40:41], v[8:9]
	v_mov_b64_e32 v[38:39], v[6:7]
	v_mov_b64_e32 v[36:37], v[4:5]
	v_mov_b64_e32 v[34:35], v[2:3]
	v_mov_b64_e32 v[62:63], v[14:15]
	v_mov_b64_e32 v[60:61], v[12:13]
	v_mov_b64_e32 v[58:59], v[10:11]
	v_mov_b64_e32 v[56:57], v[8:9]
	v_mov_b64_e32 v[54:55], v[6:7]
	v_mov_b64_e32 v[52:53], v[4:5]
	v_mov_b64_e32 v[50:51], v[2:3]
	v_mov_b32_e32 v83, v82
	v_mov_b32_e32 v84, v82
	v_mov_b32_e32 v85, v82
	v_mov_b32_e32 v86, v82
	v_mov_b32_e32 v87, v82
	v_mov_b32_e32 v88, v82
	v_mov_b32_e32 v89, v82
	v_mov_b32_e32 v90, v82
	v_mov_b32_e32 v91, v82
	v_mov_b32_e32 v92, v82
	v_mov_b32_e32 v93, v82
	v_mov_b32_e32 v94, v82
	v_mov_b32_e32 v95, v82
	v_mov_b32_e32 v96, v82
	v_mov_b32_e32 v97, v82
; #define LAS __attribute__((address_space(3)))
; __device__ __forceinline__ void finishSM(f32x16& p0, f32x16& p1, float alpha, float& l_reg, bf16x8& pa0, bf16x8& pa1, bf16x8& pa2, bf16x8& pa3) {
; #pragma unroll
;     for (int r = 0; r < 16; ++r) p1[r] = EXP_PROBE ? fmaf(p1[r], 0.001f, 1.f) : __builtin_amdgcn_exp2f(p1[r]);
;     float ps = 0.f;
; #pragma unroll
;     for (int r = 0; r < 16; ++r) ps += p0[r];
; #pragma unroll
;     for (int r = 0; r < 16; ++r) ps += p1[r];
;     { auto rr = __builtin_amdgcn_permlane32_swap(__float_as_uint(ps), __float_as_uint(ps), false, false);
;       ps = __uint_as_float(rr[0]) + __uint_as_float(rr[1]); }
;     l_reg = l_reg * alpha + ps;
;     ATT_PKN(p0, 0, pa0); ATT_PKN(p0, 8, pa1); ATT_PKN(p1, 0, pa2); ATT_PKN(p1, 8, pa3);
; }
; template <int DQK> __device__ __forceinline__ void qkt(f32x16& p0, f32x16& p1, const LAS char* buf, const bf16x8* qr, int r32, int hi, const f32x16& negm) {
; #pragma unroll
;     for (int d0 = 0; d0 < 4; ++d0) { const int ch = d0 * 2 + hi;
;         const bf16x8 b0 = *(const LAS bf16x8*)(buf + B_KN + swz64(r32, ch));
;         const bf16x8 b1 = *(const LAS bf16x8*)(buf + B_KN + swz64(32 + r32, ch));
;         p0 = __builtin_amdgcn_mfma_f32_32x32x16_bf16(b0, qr[d0], d0 == 0 ? negm : p0, 0, 0, 0);
;         p1 = __builtin_amdgcn_mfma_f32_32x32x16_bf16(b1, qr[d0], d0 == 0 ? negm : p1, 0, 0, 0); }
;     if constexpr (DQK == 96) {
; #pragma unroll
;         for (int d0 = 0; d0 < 2; ++d0) { const int ch = d0 * 2 + hi;
;             const bf16x8 b0 = *(const LAS bf16x8*)(buf + B_KR + swz32(r32, ch));
;             const bf16x8 b1 = *(const LAS bf16x8*)(buf + B_KR + swz32(32 + r32, ch));
;             p0 = __builtin_amdgcn_mfma_f32_32x32x16_bf16(b0, qr[4 + d0], p0, 0, 0, 0);
;             p1 = __builtin_amdgcn_mfma_f32_32x32x16_bf16(b1, qr[4 + d0], p1, 0, 0, 0); }
;     }
; }
; template <int DQK, bool FIXM> ...
;     ...
;         if (!NOBAR_PROBE) __syncthreads();
;         SBAR(); qkt<DQK>(pB0, pB1, lds + bK, qr, r32, hi, negm);
;         finishSM(pA0, pA1, alA, l_reg, pa0, pa1, pa2, pa3); SBAR();
;         SLOAD(1, j + 2); SBAR();
;         if constexpr (FIXM) pv_psm<true>(o0, o1, vb0 + bV, pa0, pa1, pa2, pa3, pB0, pB1, m_reg, negm, alB); else { PVO(bV); partialSM<false>(pB0, pB1, m_reg, negm, alB); }
;         SWAIT(); SWRITEO(bW, 0);
;         if (!FIXM) RESC(alB); ROT();
.LBB0_523:
	s_mov_b32 s10, s0
	s_waitcnt lgkmcnt(0)
	s_barrier
	v_add_u32_e32 v2, s13, v201
	v_add_u32_e32 v8, v2, v209
	ds_read_b128 v[4:7], v8
	ds_read_b128 v[8:11], v8 offset:4096
	v_add_u32_e32 v246, v2, v210
	ds_read_b128 v[174:177], v246
	ds_read_b128 v[246:249], v246 offset:4096
	v_add_u32_e32 v78, v2, v211
	ds_read_b128 v[250:253], v78
	ds_read_b128 v[78:81], v78 offset:4096
	v_add_u32_e32 v16, v2, v212
	ds_read_b128 v[12:15], v16
	v_add_u32_e32 v2, s13, v217
	v_exp_f32_e32 v98, v98
	v_exp_f32_e32 v99, v99
	v_exp_f32_e32 v100, v100
	v_exp_f32_e32 v101, v101
	v_exp_f32_e32 v102, v102
	v_exp_f32_e32 v103, v103
	v_exp_f32_e32 v104, v104
	v_exp_f32_e32 v105, v105
	s_waitcnt lgkmcnt(6)
	v_mfma_f32_32x32x16_bf16 v[130:145], v[4:7], v[166:169], v[82:97]
	ds_read_b128 v[4:7], v16 offset:4096
	v_exp_f32_e32 v106, v106
	v_exp_f32_e32 v107, v107
	v_exp_f32_e32 v108, v108
	v_cvt_pk_bf16_f32 v74, v243, v245
	s_waitcnt lgkmcnt(6)
	v_mfma_f32_32x32x16_bf16 v[114:129], v[8:11], v[166:169], v[82:97]
	v_add_u32_e32 v16, v2, v219
	ds_read_b128 v[8:11], v16 offset:8192
	v_exp_f32_e32 v109, v109
	v_exp_f32_e32 v110, v110
	v_exp_f32_e32 v111, v111
	v_cvt_pk_bf16_f32 v75, v241, v244
	s_waitcnt lgkmcnt(6)
	v_mfma_f32_32x32x16_bf16 v[130:145], v[174:177], v[162:165], v[130:145]
	ds_read_b128 v[174:177], v16 offset:10240
	v_exp_f32_e32 v112, v112
	v_exp_f32_e32 v113, v113
	v_cvt_pk_bf16_f32 v76, v239, v242
	v_cvt_pk_bf16_f32 v77, v238, v240
	v_add_f32_e32 v229, 0, v243
	v_add_f32_e32 v229, v245, v229
	s_waitcnt lgkmcnt(6)
	v_mfma_f32_32x32x16_bf16 v[114:129], v[246:249], v[162:165], v[114:129]
	v_add_u32_e32 v16, v2, v220
	ds_read_b128 v[246:249], v16 offset:8192
	v_cvt_pk_bf16_f32 v66, v236, v237
	v_cvt_pk_bf16_f32 v67, v233, v235
	v_add_f32_e32 v229, v241, v229
	v_add_f32_e32 v229, v244, v229
	v_add_f32_e32 v229, v239, v229
	v_add_f32_e32 v229, v242, v229
	s_waitcnt lgkmcnt(6)
	v_mfma_f32_32x32x16_bf16 v[130:145], v[250:253], v[158:161], v[130:145]
	ds_read_b128 v[250:253], v16 offset:10240
	v_cvt_pk_bf16_f32 v68, v231, v234
	v_cvt_pk_bf16_f32 v69, v230, v232
	v_add_f32_e32 v229, v238, v229
	v_add_f32_e32 v229, v240, v229
	v_add_f32_e32 v229, v236, v229
	v_add_f32_e32 v229, v237, v229
	s_waitcnt lgkmcnt(6)
	v_mfma_f32_32x32x16_bf16 v[114:129], v[78:81], v[158:161], v[114:129]
	v_add_f32_e32 v229, v233, v229
	v_add_f32_e32 v229, v235, v229
	v_add_f32_e32 v229, v231, v229
	v_add_f32_e32 v229, v234, v229
	v_add_f32_e32 v229, v230, v229
	v_add_f32_e32 v229, v232, v229
	s_waitcnt lgkmcnt(5)
	v_mfma_f32_32x32x16_bf16 v[130:145], v[12:15], v[154:157], v[130:145]
	v_add_u32_e32 v17, s11, v213
	ds_read_b64_tr_b16 v[230:231], v17 offset:0
	ds_read_b64_tr_b16 v[232:233], v17 offset:1024
	ds_read_b64_tr_b16 v[234:235], v17 offset:2048
	ds_read_b64_tr_b16 v[236:237], v17 offset:3072
	v_add_f32_e32 v229, v98, v229
	v_add_f32_e32 v229, v99, v229
	v_add_f32_e32 v229, v100, v229
	s_waitcnt lgkmcnt(8)
	v_mfma_f32_32x32x16_bf16 v[114:129], v[4:7], v[154:157], v[114:129]
	ds_read_b64_tr_b16 v[238:239], v17 offset:4096
	ds_read_b64_tr_b16 v[240:241], v17 offset:5120
	ds_read_b64_tr_b16 v[242:243], v17 offset:6144
	ds_read_b64_tr_b16 v[244:245], v17 offset:7168
	v_add_f32_e32 v229, v101, v229
	v_add_f32_e32 v229, v102, v229
	v_add_f32_e32 v229, v103, v229
	s_waitcnt lgkmcnt(11)
	v_mfma_f32_32x32x16_bf16 v[130:145], v[8:11], v[150:153], v[130:145]
	v_add_f32_e32 v229, v104, v229
	v_add_f32_e32 v229, v105, v229
	v_add_f32_e32 v229, v106, v229
	v_add_f32_e32 v229, v107, v229
	v_add_f32_e32 v229, v108, v229
	v_add_f32_e32 v229, v109, v229
	s_waitcnt lgkmcnt(10)
	v_mfma_f32_32x32x16_bf16 v[114:129], v[174:177], v[150:153], v[114:129]
	v_add_f32_e32 v229, v110, v229
	v_add_f32_e32 v229, v111, v229
	v_add_f32_e32 v229, v112, v229
	v_add_f32_e32 v228, v113, v229
	v_mov_b32_e32 v229, v228
	s_add_i32 s36, s35, -1
	s_cmp_lt_u32 s36, s30
	s_cselect_b32 s0, 0, s30
	s_cselect_b32 s1, s29, s34
	s_lshl_b32 s0, s0, 6
	s_sub_i32 s37, s1, s0
	s_lshl_b32 s1, s36, 6
	s_add_i32 s37, s37, s1
	s_lshl_b32 s0, s37, 6
	s_add_u32 s48, s44, s0
	s_addc_u32 s49, s45, 0
	s_lshl_b32 s0, s37, 11
	s_add_u32 s46, s42, s0
	s_addc_u32 s47, s43, 0
	global_load_dwordx4 v[174:177], v226, s[48:49]
	s_waitcnt lgkmcnt(9)
	v_mfma_f32_32x32x16_bf16 v[130:145], v[246:249], v[146:149], v[130:145]
	v_cvt_pk_bf16_f32 v70, v98, v99
	v_cvt_pk_bf16_f32 v71, v100, v101
	v_cvt_pk_bf16_f32 v72, v102, v103
	v_cvt_pk_bf16_f32 v73, v104, v105
	v_permlane32_swap_b32_e32 v228, v229
	global_load_dwordx4 v[8:11], v225, s[46:47]
	global_load_dwordx4 v[4:7], v225, s[46:47] offset:128
	s_waitcnt lgkmcnt(8)
	v_mfma_f32_32x32x16_bf16 v[114:129], v[250:253], v[146:149], v[114:129]
	v_cvt_pk_bf16_f32 v12, v106, v107
	v_cvt_pk_bf16_f32 v13, v108, v109
	v_cvt_pk_bf16_f32 v14, v110, v111
	v_cvt_pk_bf16_f32 v15, v112, v113
	ds_read_b64_tr_b16 v[78:79], v17 offset:512
	ds_read_b64_tr_b16 v[80:81], v17 offset:1536
	ds_read_b64_tr_b16 v[98:99], v17 offset:2560
	ds_read_b64_tr_b16 v[100:101], v17 offset:3584
	ds_read_b64_tr_b16 v[102:103], v17 offset:4608
	ds_read_b64_tr_b16 v[104:105], v17 offset:5632
	ds_read_b64_tr_b16 v[110:111], v17 offset:6656
	ds_read_b64_tr_b16 v[112:113], v17 offset:7680
	v_max3_f32 v2, v130, v131, v132
	v_max3_f32 v2, v2, v133, v134
	v_max3_f32 v2, v2, v135, v136
	v_max3_f32 v2, v2, v137, v138
	v_max3_f32 v2, v2, v139, v140
	v_max3_f32 v2, v2, v141, v142
	v_max3_f32 v2, v2, v143, v144
	v_max3_f32 v2, v2, v145, v114
	v_max3_f32 v2, v2, v115, v116
	s_waitcnt lgkmcnt(8)
	v_mfma_f32_32x32x16_bf16 v[50:65], v[230:233], v[74:77], v[50:65]
	v_max3_f32 v2, v2, v117, v118
	v_max3_f32 v2, v2, v119, v120
	v_max3_f32 v2, v2, v121, v122
	v_mfma_f32_32x32x16_bf16 v[50:65], v[234:237], v[66:69], v[50:65]
	v_max3_f32 v2, v2, v123, v124
	v_max3_f32 v2, v2, v125, v126
	v_max3_f32 v2, v2, v127, v128
	v_mfma_f32_32x32x16_bf16 v[50:65], v[238:241], v[70:73], v[50:65]
	v_max_f32_e32 v2, v2, v129
	s_nop 0
	s_nop 0
	v_mfma_f32_32x32x16_bf16 v[50:65], v[242:245], v[12:15], v[50:65]
	v_mov_b32_e32 v16, v2
	s_nop 1
	v_permlane32_swap_b32_e32 v2, v16
	v_max_f32_e32 v2, v2, v16
	v_cmp_ge_f32_e32 vcc, s28, v2
	s_cmp_eq_u64 vcc, exec
	s_cbranch_scc0 .LBB0_542
	v_mov_b32_e32 v2, 1.0
; __device__ __forceinline__ void finishSM(f32x16& p0, f32x16& p1, float alpha, float& l_reg, bf16x8& pa0, bf16x8& pa1, bf16x8& pa2, bf16x8& pa3) {
; #pragma unroll
;     for (int r = 0; r < 16; ++r) p1[r] = EXP_PROBE ? fmaf(p1[r], 0.001f, 1.f) : __builtin_amdgcn_exp2f(p1[r]);
;     float ps = 0.f;
; #pragma unroll
;     for (int r = 0; r < 16; ++r) ps += p0[r];
; #pragma unroll
;     for (int r = 0; r < 16; ++r) ps += p1[r];
;     { auto rr = __builtin_amdgcn_permlane32_swap(__float_as_uint(ps), __float_as_uint(ps), false, false);
;       ps = __uint_as_float(rr[0]) + __uint_as_float(rr[1]); }
;     l_reg = l_reg * alpha + ps;
;     ATT_PKN(p0, 0, pa0); ATT_PKN(p0, 8, pa1); ATT_PKN(p1, 0, pa2); ATT_PKN(p1, 8, pa3);
; }
; template <int DQK> __device__ __forceinline__ void qkt(f32x16& p0, f32x16& p1, const LAS char* buf, const bf16x8* qr, int r32, int hi, const f32x16& negm) {
; #pragma unroll
;     for (int d0 = 0; d0 < 4; ++d0) { const int ch = d0 * 2 + hi;
;         const bf16x8 b0 = *(const LAS bf16x8*)(buf + B_KN + swz64(r32, ch));
;         const bf16x8 b1 = *(const LAS bf16x8*)(buf + B_KN + swz64(32 + r32, ch));
;         p0 = __builtin_amdgcn_mfma_f32_32x32x16_bf16(b0, qr[d0], d0 == 0 ? negm : p0, 0, 0, 0);
;         p1 = __builtin_amdgcn_mfma_f32_32x32x16_bf16(b1, qr[d0], d0 == 0 ? negm : p1, 0, 0, 0); }
;     if constexpr (DQK == 96) {
; #pragma unroll
;         for (int d0 = 0; d0 < 2; ++d0) { const int ch = d0 * 2 + hi;
;             const bf16x8 b0 = *(const LAS bf16x8*)(buf + B_KR + swz32(r32, ch));
;             const bf16x8 b1 = *(const LAS bf16x8*)(buf + B_KR + swz32(32 + r32, ch));
; template <int DQK, bool FIXM> ...
;     ...
;         if constexpr (FIXM) pv_psm<true>(o0, o1, vb0 + bV, pa0, pa1, pa2, pa3, pB0, pB1, m_reg, negm, alB); else { PVO(bV); partialSM<false>(pB0, pB1, m_reg, negm, alB); }
;         SWAIT(); SWRITEO(bW, 0);
;         if (!FIXM) RESC(alB); ROT();
;         if (!NOBAR_PROBE) __syncthreads();
;         SBAR(); qkt<DQK>(pA0, pA1, lds + bK, qr, r32, hi, negm);
;         finishSM(pB0, pB1, alB, l_reg, pa0, pa1, pa2, pa3); SBAR();
;         if (j + 3 < NT) SLOAD(0, j + 3); SBAR();
;         if constexpr (FIXM) pv_psm<true>(o0, o1, vb0 + bV, pa0, pa1, pa2, pa3, pA0, pA1, m_reg, negm, alA); else { PVO(bV); partialSM<false>(pA0, pA1, m_reg, negm, alA); }
;         SWAIT(); SWRITEO(bW, 1);
;         if (!FIXM) RESC(alA); ROT();
.LBB0_527:
	s_waitcnt lgkmcnt(0)
	v_mfma_f32_32x32x16_bf16 v[34:49], v[78:81], v[74:77], v[34:49]
	s_waitcnt vmcnt(3)
	v_add_u32_e32 v17, s10, v187
	ds_write_b128 v17, v[178:181]
	v_add_u32_e32 v17, s10, v214
	ds_write_b128 v17, v[182:185] offset:12288
	s_cmp_eq_u64 s[2:3], 0
	s_cbranch_scc1 .Lmla_a_nokr
	v_add_u32_e32 v17, s10, v216
	ds_write_b128 v17, v[170:173] offset:8192
.Lmla_a_nokr:
	v_exp_f32_e32 v16, v130
	v_exp_f32_e32 v234, v131
	v_mfma_f32_32x32x16_bf16 v[34:49], v[98:101], v[66:69], v[34:49]
	v_exp_f32_e32 v235, v132
	v_exp_f32_e32 v236, v133
	v_exp_f32_e32 v237, v134
	v_exp_f32_e32 v238, v135
	v_mfma_f32_32x32x16_bf16 v[34:49], v[102:105], v[70:73], v[34:49]
	v_exp_f32_e32 v239, v136
	v_exp_f32_e32 v240, v137
	v_exp_f32_e32 v241, v138
	v_exp_f32_e32 v242, v139
	v_exp_f32_e32 v243, v140
	v_mfma_f32_32x32x16_bf16 v[34:49], v[110:113], v[12:15], v[34:49]
	v_exp_f32_e32 v244, v141
	v_exp_f32_e32 v245, v142
	v_exp_f32_e32 v246, v143
	v_exp_f32_e32 v247, v144
	v_exp_f32_e32 v248, v145
	v_cmp_gt_f32_e32 vcc, 1.0, v2
	s_cbranch_vccz .LBB0_531
	s_nop 7
	s_nop 7
	v_pk_mul_f32 v[64:65], v[64:65], v[2:3] op_sel_hi:[1,0]
	v_pk_mul_f32 v[62:63], v[62:63], v[2:3] op_sel_hi:[1,0]
	v_pk_mul_f32 v[60:61], v[60:61], v[2:3] op_sel_hi:[1,0]
	v_pk_mul_f32 v[58:59], v[58:59], v[2:3] op_sel_hi:[1,0]
	v_pk_mul_f32 v[56:57], v[56:57], v[2:3] op_sel_hi:[1,0]
	v_pk_mul_f32 v[54:55], v[54:55], v[2:3] op_sel_hi:[1,0]
	v_pk_mul_f32 v[52:53], v[52:53], v[2:3] op_sel_hi:[1,0]
	v_pk_mul_f32 v[50:51], v[50:51], v[2:3] op_sel_hi:[1,0]
	v_pk_mul_f32 v[48:49], v[48:49], v[2:3] op_sel_hi:[1,0]
	v_pk_mul_f32 v[46:47], v[46:47], v[2:3] op_sel_hi:[1,0]
	v_pk_mul_f32 v[44:45], v[44:45], v[2:3] op_sel_hi:[1,0]
	v_pk_mul_f32 v[42:43], v[42:43], v[2:3] op_sel_hi:[1,0]
	v_pk_mul_f32 v[40:41], v[40:41], v[2:3] op_sel_hi:[1,0]
	v_pk_mul_f32 v[38:39], v[38:39], v[2:3] op_sel_hi:[1,0]
	v_pk_mul_f32 v[36:37], v[36:37], v[2:3] op_sel_hi:[1,0]
	v_pk_mul_f32 v[34:35], v[34:35], v[2:3] op_sel_hi:[1,0]
.LBB0_531:
	s_waitcnt lgkmcnt(0)
	s_barrier
	v_add_u32_e32 v17, s10, v201
	v_add_u32_e32 v182, v17, v209
	ds_read_b128 v[178:181], v182
	ds_read_b128 v[182:185], v182 offset:4096
	v_add_u32_e32 v66, v17, v210
	ds_read_b128 v[170:173], v66
	ds_read_b128 v[66:69], v66 offset:4096
	v_add_u32_e32 v74, v17, v211
	ds_read_b128 v[70:73], v74
	ds_read_b128 v[74:77], v74 offset:4096
	v_add_u32_e32 v253, v17, v212
	ds_read_b128 v[78:81], v253
	v_add_u32_e32 v17, s10, v217
	v_exp_f32_e32 v114, v114
	v_exp_f32_e32 v115, v115
	v_exp_f32_e32 v116, v116
	v_exp_f32_e32 v117, v117
	v_exp_f32_e32 v118, v118
	v_exp_f32_e32 v119, v119
	v_exp_f32_e32 v120, v120
	v_exp_f32_e32 v121, v121
	s_waitcnt lgkmcnt(6)
	v_mfma_f32_32x32x16_bf16 v[130:145], v[178:181], v[166:169], v[82:97]
	ds_read_b128 v[178:181], v253 offset:4096
	v_exp_f32_e32 v122, v122
	v_exp_f32_e32 v123, v123
	v_exp_f32_e32 v124, v124
	v_cvt_pk_bf16_f32 v12, v16, v234
	s_waitcnt lgkmcnt(6)
	v_mfma_f32_32x32x16_bf16 v[98:113], v[182:185], v[166:169], v[82:97]
	v_add_u32_e32 v253, v17, v219
	ds_read_b128 v[182:185], v253 offset:8192
	v_exp_f32_e32 v125, v125
	v_exp_f32_e32 v126, v126
	v_exp_f32_e32 v127, v127
	v_cvt_pk_bf16_f32 v13, v235, v236
	s_waitcnt lgkmcnt(6)
	v_mfma_f32_32x32x16_bf16 v[130:145], v[170:173], v[162:165], v[130:145]
	ds_read_b128 v[170:173], v253 offset:10240
	v_exp_f32_e32 v128, v128
	v_exp_f32_e32 v129, v129
	v_cvt_pk_bf16_f32 v14, v237, v238
	v_cvt_pk_bf16_f32 v15, v239, v240
	v_add_f32_e32 v252, 0, v16
	v_add_f32_e32 v252, v234, v252
	s_waitcnt lgkmcnt(6)
	v_mfma_f32_32x32x16_bf16 v[98:113], v[66:69], v[162:165], v[98:113]
	v_add_u32_e32 v253, v17, v220
	ds_read_b128 v[66:69], v253 offset:8192
	v_cvt_pk_bf16_f32 v230, v241, v242
	v_cvt_pk_bf16_f32 v231, v243, v244
	v_add_f32_e32 v252, v235, v252
	v_add_f32_e32 v252, v236, v252
	v_add_f32_e32 v252, v237, v252
	v_add_f32_e32 v252, v238, v252
	s_waitcnt lgkmcnt(6)
	v_mfma_f32_32x32x16_bf16 v[130:145], v[70:73], v[158:161], v[130:145]
	ds_read_b128 v[70:73], v253 offset:10240
	v_cvt_pk_bf16_f32 v232, v245, v246
	v_cvt_pk_bf16_f32 v233, v247, v248
	v_add_f32_e32 v252, v239, v252
	v_add_f32_e32 v252, v240, v252
	v_add_f32_e32 v252, v241, v252
	v_add_f32_e32 v252, v242, v252
	s_waitcnt lgkmcnt(6)
	v_mfma_f32_32x32x16_bf16 v[98:113], v[74:77], v[158:161], v[98:113]
	v_add_f32_e32 v252, v243, v252
	v_add_f32_e32 v252, v244, v252
	v_add_f32_e32 v252, v245, v252
	v_add_f32_e32 v252, v246, v252
	v_add_f32_e32 v252, v247, v252
	v_add_f32_e32 v252, v248, v252
	s_waitcnt lgkmcnt(5)
	v_mfma_f32_32x32x16_bf16 v[130:145], v[78:81], v[154:157], v[130:145]
	v_add_u32_e32 v16, s13, v213
	ds_read_b64_tr_b16 v[234:235], v16 offset:0
	ds_read_b64_tr_b16 v[236:237], v16 offset:1024
	ds_read_b64_tr_b16 v[238:239], v16 offset:2048
	ds_read_b64_tr_b16 v[240:241], v16 offset:3072
	v_add_f32_e32 v252, v114, v252
	v_add_f32_e32 v252, v115, v252
	v_add_f32_e32 v252, v116, v252
	s_waitcnt lgkmcnt(8)
	v_mfma_f32_32x32x16_bf16 v[98:113], v[178:181], v[154:157], v[98:113]
	ds_read_b64_tr_b16 v[242:243], v16 offset:4096
	ds_read_b64_tr_b16 v[244:245], v16 offset:5120
	ds_read_b64_tr_b16 v[246:247], v16 offset:6144
	ds_read_b64_tr_b16 v[248:249], v16 offset:7168
	v_add_f32_e32 v252, v117, v252
	v_add_f32_e32 v252, v118, v252
	v_add_f32_e32 v252, v119, v252
	s_waitcnt lgkmcnt(11)
	v_mfma_f32_32x32x16_bf16 v[130:145], v[182:185], v[150:153], v[130:145]
	v_add_f32_e32 v252, v120, v252
	v_add_f32_e32 v252, v121, v252
	v_add_f32_e32 v252, v122, v252
	v_add_f32_e32 v252, v123, v252
	v_add_f32_e32 v252, v124, v252
	v_add_f32_e32 v252, v125, v252
	s_waitcnt lgkmcnt(10)
	v_mfma_f32_32x32x16_bf16 v[98:113], v[170:173], v[150:153], v[98:113]
	v_add_f32_e32 v252, v126, v252
	v_add_f32_e32 v252, v127, v252
	v_add_f32_e32 v252, v128, v252
	s_waitcnt lgkmcnt(9)
	v_mfma_f32_32x32x16_bf16 v[130:145], v[66:69], v[146:149], v[130:145]
	v_cvt_pk_bf16_f32 v114, v114, v115
	v_cvt_pk_bf16_f32 v115, v116, v117
	v_cvt_pk_bf16_f32 v116, v118, v119
	v_cvt_pk_bf16_f32 v117, v120, v121
	s_cmp_ge_u32 s35, s31
	s_cbranch_scc1 .Lmla_b_noload
	s_cmp_lt_u32 s35, s30
	s_cselect_b32 s0, 0, s30
	s_cselect_b32 s1, s29, s34
	s_lshl_b32 s0, s0, 6
	s_sub_i32 s37, s1, s0
	s_lshl_b32 s1, s35, 6
	s_add_i32 s37, s37, s1
	s_lshl_b32 s0, s37, 6
	s_add_u32 s48, s44, s0
	s_addc_u32 s49, s45, 0
	s_lshl_b32 s0, s37, 11
	s_add_u32 s46, s42, s0
	s_addc_u32 s47, s43, 0
	global_load_dwordx4 v[170:173], v226, s[48:49]
	global_load_dwordx4 v[178:181], v225, s[46:47]
	global_load_dwordx4 v[182:185], v225, s[46:47] offset:128
; #define SWRITEO(boff, i) do { *(LAS bf16x8*)(lds + (boff) + kn_st) = skn[i]; *(LAS bf16x8*)(lds + (boff) + v_stw) = sv[i]; if (krw) *(LAS bf16x8*)(lds + (boff) + kr_st) = skr[i]; } while (0)
; #define PVO(boff) do { pv_one<0>(o0, vb0 + (boff), pa0, pa1, pa2, pa3); pv_one<1>(o1, vb0 + (boff), pa0, pa1, pa2, pa3); } while (0)
; #define SWAIT() asm volatile("s_waitcnt vmcnt(2)" ::: "memory")
; #define RESC(a) do { if (__any((a) < 1.f)) { _Pragma("unroll") for (int r = 0; r < 16; ++r) { o0[r] *= (a); o1[r] *= (a); } } } while (0)
; #define ROT() do { const int _t = bV; bV = bK; bK = bW; bW = _t; } while (0)
; __device__ __forceinline__ float psm_max(const f32x16& p0, const f32x16& p1) {
;     float pmax = p0[0];
; #pragma unroll
;     for (int r = 1; r < 16; ++r) pmax = fmaxf(pmax, p0[r]);
; #pragma unroll
;     for (int r = 0; r < 16; ++r) pmax = fmaxf(pmax, p1[r]);
;     { auto rr = __builtin_amdgcn_permlane32_swap(__float_as_uint(pmax), __float_as_uint(pmax), false, false);
;       pmax = fmaxf(__uint_as_float(rr[0]), __uint_as_float(rr[1])); }
;     return pmax;
; }
; template <bool FIRST> __device__ __forceinline__ void psm_apply(f32x16& p0, f32x16& p1, float pmax, float& m_reg, f32x16& negm, float& alpha) {
;     alpha = 1.f;
;     if (FIRST || !__builtin_expect(__all(pmax <= THR2), 1)) {
;         const float delta = FIRST ? pmax : fmaxf(pmax, 0.f);
;         if (!FIRST) alpha = __builtin_amdgcn_exp2f(-delta);
;         m_reg += delta;
; #pragma unroll
;         for (int r = 0; r < 16; ++r) { p0[r] -= delta; p1[r] -= delta; negm[r] = -m_reg; }
;     }
; #pragma unroll
;     for (int r = 0; r < 16; ++r) p0[r] = EXP_PROBE ? fmaf(p0[r], 0.001f, 1.f) : __builtin_amdgcn_exp2f(p0[r]);
; }
; template <bool FIRST> __device__ __forceinline__ void partialSM(f32x16& p0, f32x16& p1, float& m_reg, f32x16& negm, float& alpha) {
;     const float pmax = psm_max(p0, p1); psm_apply<FIRST>(p0, p1, pmax, m_reg, negm, alpha);
; }
; template <int DQK, bool FIXM> ...
;     ...
;         if constexpr (FIXM) pv_psm<true>(o0, o1, vb0 + bV, pa0, pa1, pa2, pa3, pA0, pA1, m_reg, negm, alA); else { PVO(bV); partialSM<false>(pA0, pA1, m_reg, negm, alA); }
;         SWAIT(); SWRITEO(bW, 1);
;         if (!FIXM) RESC(alA); ROT();
;     }
.Lmla_b_ld_done:
	s_waitcnt lgkmcnt(8)
	v_mfma_f32_32x32x16_bf16 v[98:113], v[70:73], v[146:149], v[98:113]
	v_cvt_pk_bf16_f32 v118, v122, v123
	v_cvt_pk_bf16_f32 v119, v124, v125
	v_cvt_pk_bf16_f32 v120, v126, v127
	v_cvt_pk_bf16_f32 v121, v128, v129
	v_add_f32_e32 v126, v129, v252
	v_mov_b32_e32 v127, v126
	ds_read_b64_tr_b16 v[66:67], v16 offset:512
	ds_read_b64_tr_b16 v[68:69], v16 offset:1536
	ds_read_b64_tr_b16 v[70:71], v16 offset:2560
	ds_read_b64_tr_b16 v[72:73], v16 offset:3584
	ds_read_b64_tr_b16 v[74:75], v16 offset:4608
	ds_read_b64_tr_b16 v[76:77], v16 offset:5632
	ds_read_b64_tr_b16 v[78:79], v16 offset:6656
	ds_read_b64_tr_b16 v[80:81], v16 offset:7680
	v_permlane32_swap_b32_e32 v126, v127
	v_max3_f32 v250, v130, v131, v132
	v_max3_f32 v250, v250, v133, v134
	v_max3_f32 v250, v250, v135, v136
	v_max3_f32 v250, v250, v137, v138
	v_max3_f32 v250, v250, v139, v140
	v_max3_f32 v250, v250, v141, v142
	v_max3_f32 v250, v250, v143, v144
	v_max3_f32 v250, v250, v145, v98
	v_max3_f32 v250, v250, v99, v100
	s_waitcnt lgkmcnt(8)
	v_mfma_f32_32x32x16_bf16 v[50:65], v[234:237], v[12:15], v[50:65]
	v_max3_f32 v250, v250, v101, v102
	v_max3_f32 v250, v250, v103, v104
	v_max3_f32 v250, v250, v105, v106
	v_mfma_f32_32x32x16_bf16 v[50:65], v[238:241], v[230:233], v[50:65]
	v_max3_f32 v250, v250, v107, v108
	v_max3_f32 v250, v250, v109, v110
	v_max3_f32 v250, v250, v111, v112
	v_mfma_f32_32x32x16_bf16 v[50:65], v[242:245], v[114:117], v[50:65]
	v_max_f32_e32 v250, v250, v113
	s_nop 0
	s_nop 0
	v_mfma_f32_32x32x16_bf16 v[50:65], v[246:249], v[118:121], v[50:65]
	v_mov_b32_e32 v251, v250
	s_nop 1
	v_permlane32_swap_b32_e32 v250, v251
	v_max_f32_e32 v250, v250, v251
	v_cmp_ge_f32_e32 vcc, s28, v250
	s_cmp_eq_u64 vcc, exec
	v_mov_b32_e32 v16, 1.0
	s_cbranch_scc0 .LBB0_543
.LBB0_536:
	s_waitcnt lgkmcnt(0)
	v_mfma_f32_32x32x16_bf16 v[34:49], v[66:69], v[12:15], v[34:49]
	s_waitcnt vmcnt(3)
	v_add_u32_e32 v253, s11, v187
	ds_write_b128 v253, v[8:11]
	v_add_u32_e32 v253, s11, v214
	ds_write_b128 v253, v[4:7] offset:12288
	s_cmp_eq_u64 s[2:3], 0
	s_cbranch_scc1 .Lmla_b_nokr
	v_add_u32_e32 v253, s11, v216
	ds_write_b128 v253, v[174:177] offset:8192
.Lmla_b_nokr:
	v_exp_f32_e32 v243, v130
	v_exp_f32_e32 v245, v131
	v_mfma_f32_32x32x16_bf16 v[34:49], v[70:73], v[230:233], v[34:49]
	v_exp_f32_e32 v241, v132
	v_exp_f32_e32 v244, v133
	v_exp_f32_e32 v239, v134
	v_exp_f32_e32 v242, v135
	v_mfma_f32_32x32x16_bf16 v[34:49], v[74:77], v[114:117], v[34:49]
	v_exp_f32_e32 v238, v136
	v_exp_f32_e32 v240, v137
	v_exp_f32_e32 v236, v138
	v_exp_f32_e32 v237, v139
	v_exp_f32_e32 v235, v141
	v_mfma_f32_32x32x16_bf16 v[34:49], v[78:81], v[118:121], v[34:49]
	v_exp_f32_e32 v234, v143
	v_exp_f32_e32 v233, v140
	v_exp_f32_e32 v231, v142
	v_exp_f32_e32 v230, v144
	v_exp_f32_e32 v232, v145
	v_cmp_gt_f32_e32 vcc, 1.0, v16
	s_cbranch_vccz .LBB0_540
	s_nop 7
	s_nop 7
	v_pk_mul_f32 v[64:65], v[64:65], v[16:17] op_sel_hi:[1,0]
	v_pk_mul_f32 v[62:63], v[62:63], v[16:17] op_sel_hi:[1,0]
	v_pk_mul_f32 v[60:61], v[60:61], v[16:17] op_sel_hi:[1,0]
	v_pk_mul_f32 v[58:59], v[58:59], v[16:17] op_sel_hi:[1,0]
	v_pk_mul_f32 v[56:57], v[56:57], v[16:17] op_sel_hi:[1,0]
	v_pk_mul_f32 v[54:55], v[54:55], v[16:17] op_sel_hi:[1,0]
	v_pk_mul_f32 v[52:53], v[52:53], v[16:17] op_sel_hi:[1,0]
	v_pk_mul_f32 v[50:51], v[50:51], v[16:17] op_sel_hi:[1,0]
	v_pk_mul_f32 v[48:49], v[48:49], v[16:17] op_sel_hi:[1,0]
	v_pk_mul_f32 v[46:47], v[46:47], v[16:17] op_sel_hi:[1,0]
	v_pk_mul_f32 v[44:45], v[44:45], v[16:17] op_sel_hi:[1,0]
	v_pk_mul_f32 v[42:43], v[42:43], v[16:17] op_sel_hi:[1,0]
	v_pk_mul_f32 v[40:41], v[40:41], v[16:17] op_sel_hi:[1,0]
	v_pk_mul_f32 v[38:39], v[38:39], v[16:17] op_sel_hi:[1,0]
	v_pk_mul_f32 v[36:37], v[36:37], v[16:17] op_sel_hi:[1,0]
	v_pk_mul_f32 v[34:35], v[34:35], v[16:17] op_sel_hi:[1,0]
.LBB0_540:
	v_add_f32_e32 v4, v228, v229
	v_fmac_f32_e32 v4, v227, v223
	v_add_f32_e32 v223, v126, v127
	s_add_i32 s35, s35, 2
	v_fmac_f32_e32 v223, v4, v2
	s_mov_b32 s37, s11
	s_cmp_ge_u32 s36, s12
	s_cbranch_scc1 .Lmla_exit
	s_mov_b32 s0, s13
	s_mov_b32 s13, s11
	s_mov_b32 s11, s10
	v_mov_b32_e32 v227, v16
	s_branch .LBB0_523

; template <bool FIRST> __device__ __forceinline__ void psm_apply(f32x16& p0, f32x16& p1, float pmax, float& m_reg, f32x16& negm, float& alpha) {
;     alpha = 1.f;
;     if (FIRST || !__builtin_expect(__all(pmax <= THR2), 1)) {
;         const float delta = FIRST ? pmax : fmaxf(pmax, 0.f);
;         if (!FIRST) alpha = __builtin_amdgcn_exp2f(-delta);
;         m_reg += delta;
; #pragma unroll
;         for (int r = 0; r < 16; ++r) { p0[r] -= delta; p1[r] -= delta; negm[r] = -m_reg; }
;     }
.LBB0_543:
	v_max_f32_e32 v250, v250, v250
	v_max_f32_e32 v250, 0, v250
	v_exp_f32_e64 v16, -v250
	v_add_f32_e32 v224, v224, v250
	v_xor_b32_e32 v82, 0x80000000, v224
	v_pk_add_f32 v[130:131], v[130:131], v[250:251] op_sel_hi:[1,0] neg_lo:[0,1] neg_hi:[0,1]
	v_pk_add_f32 v[132:133], v[132:133], v[250:251] op_sel_hi:[1,0] neg_lo:[0,1] neg_hi:[0,1]
	v_pk_add_f32 v[134:135], v[134:135], v[250:251] op_sel_hi:[1,0] neg_lo:[0,1] neg_hi:[0,1]
	v_pk_add_f32 v[136:137], v[136:137], v[250:251] op_sel_hi:[1,0] neg_lo:[0,1] neg_hi:[0,1]
	v_pk_add_f32 v[138:139], v[138:139], v[250:251] op_sel_hi:[1,0] neg_lo:[0,1] neg_hi:[0,1]
	v_pk_add_f32 v[140:141], v[140:141], v[250:251] op_sel_hi:[1,0] neg_lo:[0,1] neg_hi:[0,1]
	v_pk_add_f32 v[142:143], v[142:143], v[250:251] op_sel_hi:[1,0] neg_lo:[0,1] neg_hi:[0,1]
	v_pk_add_f32 v[144:145], v[144:145], v[250:251] op_sel_hi:[1,0] neg_lo:[0,1] neg_hi:[0,1]
	v_sub_f32_e32 v113, v113, v250
	v_sub_f32_e32 v112, v112, v250
	v_sub_f32_e32 v111, v111, v250
	v_sub_f32_e32 v110, v110, v250
	v_sub_f32_e32 v109, v109, v250
	v_sub_f32_e32 v108, v108, v250
	v_sub_f32_e32 v107, v107, v250
	v_sub_f32_e32 v106, v106, v250
	v_sub_f32_e32 v105, v105, v250
	v_sub_f32_e32 v104, v104, v250
	v_sub_f32_e32 v103, v103, v250
	v_sub_f32_e32 v102, v102, v250
	v_sub_f32_e32 v101, v101, v250
	v_sub_f32_e32 v100, v100, v250
	v_sub_f32_e32 v99, v99, v250
	v_sub_f32_e32 v98, v98, v250
	v_mov_b32_e32 v83, v82
	v_mov_b32_e32 v84, v82
	v_mov_b32_e32 v85, v82
	v_mov_b32_e32 v86, v82
	v_mov_b32_e32 v87, v82
	v_mov_b32_e32 v88, v82
	v_mov_b32_e32 v89, v82
	v_mov_b32_e32 v90, v82
	v_mov_b32_e32 v91, v82
	v_mov_b32_e32 v92, v82
	v_mov_b32_e32 v93, v82
	v_mov_b32_e32 v94, v82
	v_mov_b32_e32 v95, v82
	v_mov_b32_e32 v96, v82
	v_mov_b32_e32 v97, v82
	s_branch .LBB0_536
